# A/B on the in-proj GEMM: per-segment s_setprio flips deleted, one static s_setprio 1 for waves 4-7 for the phase (other GEMM phases unchanged)
# baseline (speedup 1.0000x reference)
.LBB0_124:
	s_add_i32 s79, s56, 2
	s_add_u32 s58, s54, 0x80
	s_addc_u32 s57, s55, 0
	s_cmp_eq_u32 s70, s56
	s_cselect_b32 s57, s41, s57
	s_cselect_b32 s56, s40, s58
	s_cselect_b32 s59, s53, s78
	s_cselect_b32 s58, s52, s77
	s_add_i32 s80, 0, 0x10000
	s_add_i32 s81, 0, 0x14000
	v_add_u32_e32 v2, s80, v183
	v_add_u32_e32 v14, s81, v183
	ds_read_b128 v[18:21], v2
	ds_read_b128 v[22:25], v2 offset:1024
	ds_read_b128 v[26:29], v2 offset:2048
	ds_read_b128 v[30:33], v2 offset:3072
	ds_read_b128 v[2:5], v14
	ds_read_b128 v[6:9], v14 offset:1024
	ds_read_b128 v[10:13], v14 offset:2048
	ds_read_b128 v[14:17], v14 offset:3072
	v_lshl_add_u64 v[176:177], s[54:55], 0, v[164:165]
	s_add_i32 m0, s62, 0xc000
	ds_read_b128 v[168:171], v184
	ds_read_b128 v[172:175], v184 offset:1024
	ds_read_b128 v[186:189], v184 offset:2048
	ds_read_b128 v[190:193], v184 offset:3072
	ds_read_b128 v[194:197], v184 offset:4096
	ds_read_b128 v[198:201], v184 offset:5120
	ds_read_b128 v[202:205], v184 offset:6144
	ds_read_b128 v[206:209], v184 offset:7168
	global_load_lds_dwordx4 v[176:177], off
	v_lshl_add_u64 v[176:177], s[54:55], 0, v[166:167]
	s_add_i32 m0, s62, 0xe000
	s_nop 0
	global_load_lds_dwordx4 v[176:177], off
	s_waitcnt vmcnt(8)
	s_waitcnt lgkmcnt(0)
	s_barrier
	s_waitcnt lgkmcnt(0)
	v_mfma_scale_f32_16x16x128_f8f6f4 v[154:157], v[18:25], v[168:175], v[154:157], v180, v180 op_sel_hi:[0,0,0]
	v_mfma_scale_f32_16x16x128_f8f6f4 v[158:161], v[26:33], v[168:175], v[158:161], v180, v180 op_sel_hi:[0,0,0]
	v_mfma_scale_f32_16x16x128_f8f6f4 v[142:145], v[18:25], v[186:193], v[142:145], v180, v180 op_sel_hi:[0,0,0]
	v_mfma_scale_f32_16x16x128_f8f6f4 v[138:141], v[26:33], v[186:193], v[138:141], v180, v180 op_sel_hi:[0,0,0]
	v_mfma_scale_f32_16x16x128_f8f6f4 v[126:129], v[18:25], v[194:201], v[126:129], v180, v180 op_sel_hi:[0,0,0]
	v_mfma_scale_f32_16x16x128_f8f6f4 v[122:125], v[26:33], v[194:201], v[122:125], v180, v180 op_sel_hi:[0,0,0]
	v_mfma_scale_f32_16x16x128_f8f6f4 v[110:113], v[18:25], v[202:209], v[110:113], v180, v180 op_sel_hi:[0,0,0]
	v_mfma_scale_f32_16x16x128_f8f6f4 v[106:109], v[26:33], v[202:209], v[106:109], v180, v180 op_sel_hi:[0,0,0]
	v_mfma_scale_f32_16x16x128_f8f6f4 v[150:153], v[2:9], v[168:175], v[150:153], v180, v180 op_sel_hi:[0,0,0]
	v_mfma_scale_f32_16x16x128_f8f6f4 v[146:149], v[10:17], v[168:175], v[146:149], v180, v180 op_sel_hi:[0,0,0]
	v_mfma_scale_f32_16x16x128_f8f6f4 v[134:137], v[2:9], v[186:193], v[134:137], v180, v180 op_sel_hi:[0,0,0]
	v_mfma_scale_f32_16x16x128_f8f6f4 v[130:133], v[10:17], v[186:193], v[130:133], v180, v180 op_sel_hi:[0,0,0]
	v_mfma_scale_f32_16x16x128_f8f6f4 v[118:121], v[2:9], v[194:201], v[118:121], v180, v180 op_sel_hi:[0,0,0]
	v_mfma_scale_f32_16x16x128_f8f6f4 v[114:117], v[10:17], v[194:201], v[114:117], v180, v180 op_sel_hi:[0,0,0]
	v_mfma_scale_f32_16x16x128_f8f6f4 v[102:105], v[2:9], v[202:209], v[102:105], v180, v180 op_sel_hi:[0,0,0]
	v_mfma_scale_f32_16x16x128_f8f6f4 v[98:101], v[10:17], v[202:209], v[98:101], v180, v180 op_sel_hi:[0,0,0]
	s_barrier
	s_add_i32 s80, s80, s20
	v_lshl_add_u64 v[168:169], s[58:59], 0, v[0:1]
	s_mov_b32 m0, s80
	ds_read_b128 v[186:189], v184 offset:16384
	ds_read_b128 v[190:193], v184 offset:17408
	ds_read_b128 v[194:197], v184 offset:18432
	ds_read_b128 v[198:201], v184 offset:19456
	ds_read_b128 v[202:205], v184 offset:20480
	ds_read_b128 v[206:209], v184 offset:21504
	ds_read_b128 v[212:215], v184 offset:22528
	ds_read_b128 v[216:219], v184 offset:23552
	global_load_lds_dwordx4 v[168:169], off
	s_add_i32 m0, s80, 0x2000
	s_add_u32 s58, s58, s8
	s_addc_u32 s59, s59, s9
	v_lshl_add_u64 v[170:171], v[168:169], 0, s[6:7]
	v_lshl_add_u64 v[172:173], s[58:59], 0, v[0:1]
	s_add_i32 s58, s81, s20
	global_load_lds_dwordx4 v[170:171], off
	s_mov_b32 m0, s58
	v_lshl_add_u64 v[174:175], v[172:173], 0, s[6:7]
	global_load_lds_dwordx4 v[172:173], off
	s_add_i32 m0, s58, 0x2000
	v_lshl_add_u64 v[176:177], s[56:57], 0, v[162:163]
	global_load_lds_dwordx4 v[174:175], off
	s_mov_b32 m0, s62
	v_lshl_add_u64 v[178:179], v[176:177], 0, s[6:7]
	global_load_lds_dwordx4 v[176:177], off
	s_mov_b32 m0, s63
	s_nop 0
	global_load_lds_dwordx4 v[178:179], off
	s_waitcnt vmcnt(8)
	s_waitcnt lgkmcnt(0)
	s_barrier
	s_waitcnt lgkmcnt(0)
	v_mfma_scale_f32_16x16x128_f8f6f4 v[94:97], v[18:25], v[186:193], v[94:97], v180, v180 op_sel_hi:[0,0,0]
	v_mfma_scale_f32_16x16x128_f8f6f4 v[90:93], v[26:33], v[186:193], v[90:93], v180, v180 op_sel_hi:[0,0,0]
	v_mfma_scale_f32_16x16x128_f8f6f4 v[78:81], v[18:25], v[194:201], v[78:81], v180, v180 op_sel_hi:[0,0,0]
	v_mfma_scale_f32_16x16x128_f8f6f4 v[74:77], v[26:33], v[194:201], v[74:77], v180, v180 op_sel_hi:[0,0,0]
	v_mfma_scale_f32_16x16x128_f8f6f4 v[62:65], v[18:25], v[202:209], v[62:65], v180, v180 op_sel_hi:[0,0,0]
	v_mfma_scale_f32_16x16x128_f8f6f4 v[58:61], v[26:33], v[202:209], v[58:61], v180, v180 op_sel_hi:[0,0,0]
	v_mfma_scale_f32_16x16x128_f8f6f4 v[46:49], v[18:25], v[212:219], v[46:49], v180, v180 op_sel_hi:[0,0,0]
	v_mfma_scale_f32_16x16x128_f8f6f4 v[42:45], v[26:33], v[212:219], v[42:45], v180, v180 op_sel_hi:[0,0,0]
	v_mfma_scale_f32_16x16x128_f8f6f4 v[86:89], v[2:9], v[186:193], v[86:89], v180, v180 op_sel_hi:[0,0,0]
	v_mfma_scale_f32_16x16x128_f8f6f4 v[82:85], v[10:17], v[186:193], v[82:85], v180, v180 op_sel_hi:[0,0,0]
	v_mfma_scale_f32_16x16x128_f8f6f4 v[70:73], v[2:9], v[194:201], v[70:73], v180, v180 op_sel_hi:[0,0,0]
	v_mfma_scale_f32_16x16x128_f8f6f4 v[66:69], v[10:17], v[194:201], v[66:69], v180, v180 op_sel_hi:[0,0,0]
	v_mfma_scale_f32_16x16x128_f8f6f4 v[54:57], v[2:9], v[202:209], v[54:57], v180, v180 op_sel_hi:[0,0,0]
	v_mfma_scale_f32_16x16x128_f8f6f4 v[50:53], v[10:17], v[202:209], v[50:53], v180, v180 op_sel_hi:[0,0,0]
	v_mfma_scale_f32_16x16x128_f8f6f4 v[38:41], v[2:9], v[212:219], v[38:41], v180, v180 op_sel_hi:[0,0,0]
	v_mfma_scale_f32_16x16x128_f8f6f4 v[34:37], v[10:17], v[212:219], v[34:37], v180, v180 op_sel_hi:[0,0,0]
	s_barrier
	s_add_i32 s58, 0, 0x18000
	s_add_i32 s59, 0, 0x1c000
	v_add_u32_e32 v14, s58, v183
	v_add_u32_e32 v30, s59, v183
	ds_read_b128 v[2:5], v14
	ds_read_b128 v[6:9], v14 offset:1024
	ds_read_b128 v[10:13], v14 offset:2048
	ds_read_b128 v[14:17], v14 offset:3072
	ds_read_b128 v[18:21], v30
	ds_read_b128 v[22:25], v30 offset:1024
	ds_read_b128 v[26:29], v30 offset:2048
	ds_read_b128 v[30:33], v30 offset:3072
	s_add_u32 s56, s56, s8
	s_addc_u32 s57, s57, s9
	s_mov_b32 m0, s64
	v_lshl_add_u64 v[220:221], s[56:57], 0, v[162:163]
	ds_read_b128 v[186:189], v184 offset:32768
	ds_read_b128 v[190:193], v184 offset:33792
	ds_read_b128 v[194:197], v184 offset:34816
	ds_read_b128 v[198:201], v184 offset:35840
	ds_read_b128 v[202:205], v184 offset:36864
	ds_read_b128 v[206:209], v184 offset:37888
	ds_read_b128 v[212:215], v184 offset:38912
	ds_read_b128 v[216:219], v184 offset:39936
	global_load_lds_dwordx4 v[220:221], off
	v_lshl_add_u64 v[220:221], v[220:221], 0, s[6:7]
	s_mov_b32 m0, s65
	s_nop 0
	global_load_lds_dwordx4 v[220:221], off
	s_waitcnt vmcnt(8)
	s_waitcnt lgkmcnt(0)
	s_barrier
	s_waitcnt lgkmcnt(0)
	v_mfma_scale_f32_16x16x128_f8f6f4 v[154:157], v[2:9], v[186:193], v[154:157], v180, v180 op_sel_hi:[0,0,0]
	v_mfma_scale_f32_16x16x128_f8f6f4 v[158:161], v[10:17], v[186:193], v[158:161], v180, v180 op_sel_hi:[0,0,0]
	v_mfma_scale_f32_16x16x128_f8f6f4 v[142:145], v[2:9], v[194:201], v[142:145], v180, v180 op_sel_hi:[0,0,0]
	v_mfma_scale_f32_16x16x128_f8f6f4 v[138:141], v[10:17], v[194:201], v[138:141], v180, v180 op_sel_hi:[0,0,0]
	v_mfma_scale_f32_16x16x128_f8f6f4 v[126:129], v[2:9], v[202:209], v[126:129], v180, v180 op_sel_hi:[0,0,0]
	v_mfma_scale_f32_16x16x128_f8f6f4 v[122:125], v[10:17], v[202:209], v[122:125], v180, v180 op_sel_hi:[0,0,0]
	v_mfma_scale_f32_16x16x128_f8f6f4 v[110:113], v[2:9], v[212:219], v[110:113], v180, v180 op_sel_hi:[0,0,0]
	v_mfma_scale_f32_16x16x128_f8f6f4 v[106:109], v[10:17], v[212:219], v[106:109], v180, v180 op_sel_hi:[0,0,0]
	v_mfma_scale_f32_16x16x128_f8f6f4 v[150:153], v[18:25], v[186:193], v[150:153], v180, v180 op_sel_hi:[0,0,0]
	v_mfma_scale_f32_16x16x128_f8f6f4 v[146:149], v[26:33], v[186:193], v[146:149], v180, v180 op_sel_hi:[0,0,0]
	v_mfma_scale_f32_16x16x128_f8f6f4 v[134:137], v[18:25], v[194:201], v[134:137], v180, v180 op_sel_hi:[0,0,0]
	v_mfma_scale_f32_16x16x128_f8f6f4 v[130:133], v[26:33], v[194:201], v[130:133], v180, v180 op_sel_hi:[0,0,0]
	v_mfma_scale_f32_16x16x128_f8f6f4 v[118:121], v[18:25], v[202:209], v[118:121], v180, v180 op_sel_hi:[0,0,0]
	v_mfma_scale_f32_16x16x128_f8f6f4 v[114:117], v[26:33], v[202:209], v[114:117], v180, v180 op_sel_hi:[0,0,0]
	v_mfma_scale_f32_16x16x128_f8f6f4 v[102:105], v[18:25], v[212:219], v[102:105], v180, v180 op_sel_hi:[0,0,0]
	v_mfma_scale_f32_16x16x128_f8f6f4 v[98:101], v[26:33], v[212:219], v[98:101], v180, v180 op_sel_hi:[0,0,0]
	s_barrier
	s_add_i32 s56, s58, s20
	v_lshl_add_u64 v[168:169], v[168:169], 0, s[36:37]
	s_mov_b32 m0, s56
	ds_read_b128 v[186:189], v184 offset:49152
	ds_read_b128 v[190:193], v184 offset:50176
	ds_read_b128 v[194:197], v184 offset:51200
	ds_read_b128 v[198:201], v184 offset:52224
	ds_read_b128 v[202:205], v184 offset:53248
	ds_read_b128 v[206:209], v184 offset:54272
	ds_read_b128 v[212:215], v184 offset:55296
	ds_read_b128 v[216:219], v184 offset:56320
	global_load_lds_dwordx4 v[168:169], off
	v_lshl_add_u64 v[168:169], v[170:171], 0, s[36:37]
	s_add_i32 m0, s56, 0x2000
	s_add_i32 s56, s59, s20
	global_load_lds_dwordx4 v[168:169], off
	v_lshl_add_u64 v[168:169], v[172:173], 0, s[36:37]
	s_mov_b32 m0, s56
	s_nop 0
	global_load_lds_dwordx4 v[168:169], off
	v_lshl_add_u64 v[168:169], v[174:175], 0, s[36:37]
	s_add_i32 m0, s56, 0x2000
	s_nop 0
	global_load_lds_dwordx4 v[168:169], off
	v_lshl_add_u64 v[168:169], v[176:177], 0, s[36:37]
	s_mov_b32 m0, s66
	s_nop 0
	global_load_lds_dwordx4 v[168:169], off
	v_lshl_add_u64 v[168:169], v[178:179], 0, s[36:37]
	s_mov_b32 m0, s67
	s_nop 0
	global_load_lds_dwordx4 v[168:169], off
	s_waitcnt vmcnt(8)
	s_waitcnt lgkmcnt(0)
	s_barrier
	s_waitcnt lgkmcnt(0)
	v_mfma_scale_f32_16x16x128_f8f6f4 v[94:97], v[2:9], v[186:193], v[94:97], v180, v180 op_sel_hi:[0,0,0]
	v_mfma_scale_f32_16x16x128_f8f6f4 v[90:93], v[10:17], v[186:193], v[90:93], v180, v180 op_sel_hi:[0,0,0]
	v_mfma_scale_f32_16x16x128_f8f6f4 v[78:81], v[2:9], v[194:201], v[78:81], v180, v180 op_sel_hi:[0,0,0]
	v_mfma_scale_f32_16x16x128_f8f6f4 v[74:77], v[10:17], v[194:201], v[74:77], v180, v180 op_sel_hi:[0,0,0]
	v_mfma_scale_f32_16x16x128_f8f6f4 v[62:65], v[2:9], v[202:209], v[62:65], v180, v180 op_sel_hi:[0,0,0]
	v_mfma_scale_f32_16x16x128_f8f6f4 v[58:61], v[10:17], v[202:209], v[58:61], v180, v180 op_sel_hi:[0,0,0]
	v_mfma_scale_f32_16x16x128_f8f6f4 v[46:49], v[2:9], v[212:219], v[46:49], v180, v180 op_sel_hi:[0,0,0]
	v_mfma_scale_f32_16x16x128_f8f6f4 v[42:45], v[10:17], v[212:219], v[42:45], v180, v180 op_sel_hi:[0,0,0]
	v_mfma_scale_f32_16x16x128_f8f6f4 v[86:89], v[18:25], v[186:193], v[86:89], v180, v180 op_sel_hi:[0,0,0]
	v_mfma_scale_f32_16x16x128_f8f6f4 v[82:85], v[26:33], v[186:193], v[82:85], v180, v180 op_sel_hi:[0,0,0]
	v_mfma_scale_f32_16x16x128_f8f6f4 v[70:73], v[18:25], v[194:201], v[70:73], v180, v180 op_sel_hi:[0,0,0]
	v_mfma_scale_f32_16x16x128_f8f6f4 v[66:69], v[26:33], v[194:201], v[66:69], v180, v180 op_sel_hi:[0,0,0]
	v_mfma_scale_f32_16x16x128_f8f6f4 v[54:57], v[18:25], v[202:209], v[54:57], v180, v180 op_sel_hi:[0,0,0]
	v_mfma_scale_f32_16x16x128_f8f6f4 v[50:53], v[26:33], v[202:209], v[50:53], v180, v180 op_sel_hi:[0,0,0]
	v_mfma_scale_f32_16x16x128_f8f6f4 v[38:41], v[18:25], v[212:219], v[38:41], v180, v180 op_sel_hi:[0,0,0]
	v_mfma_scale_f32_16x16x128_f8f6f4 v[34:37], v[26:33], v[212:219], v[34:37], v180, v180 op_sel_hi:[0,0,0]
	s_barrier
	s_add_u32 s54, s54, 0x100
	s_addc_u32 s55, s55, 0
	s_add_u32 s77, s77, 0x100
	s_addc_u32 s78, s78, 0
	s_cmp_ge_i32 s79, s30
	s_mov_b32 s56, s79
	s_cbranch_scc0 .LBB0_124

.LBB0_145:
	s_add_i32 s79, s56, 2
	s_add_u32 s58, s54, 0x80
	s_addc_u32 s57, s55, 0
	s_cmp_eq_u32 s73, s56
	s_cselect_b32 s57, s41, s57
	s_cselect_b32 s56, s40, s58
	s_cselect_b32 s59, s53, s78
	s_cselect_b32 s58, s52, s70
	s_add_i32 s80, 0, 0x10000
	s_add_i32 s81, 0, 0x14000
	v_add_u32_e32 v2, s80, v182
	v_add_u32_e32 v14, s81, v182
	ds_read_b128 v[18:21], v2
	ds_read_b128 v[22:25], v2 offset:1024
	ds_read_b128 v[26:29], v2 offset:2048
	ds_read_b128 v[30:33], v2 offset:3072
	ds_read_b128 v[2:5], v14
	ds_read_b128 v[6:9], v14 offset:1024
	ds_read_b128 v[10:13], v14 offset:2048
	ds_read_b128 v[14:17], v14 offset:3072
	v_lshl_add_u64 v[176:177], s[54:55], 0, v[164:165]
	s_add_i32 m0, s64, 0xc000
	ds_read_b128 v[168:171], v183
	ds_read_b128 v[172:175], v183 offset:1024
	ds_read_b128 v[184:187], v183 offset:2048
	ds_read_b128 v[188:191], v183 offset:3072
	ds_read_b128 v[192:195], v183 offset:4096
	ds_read_b128 v[196:199], v183 offset:5120
	ds_read_b128 v[200:203], v183 offset:6144
	ds_read_b128 v[204:207], v183 offset:7168
	global_load_lds_dwordx4 v[176:177], off
	v_lshl_add_u64 v[176:177], s[54:55], 0, v[166:167]
	s_add_i32 m0, s64, 0xe000
	s_nop 0
	global_load_lds_dwordx4 v[176:177], off
	s_waitcnt vmcnt(8)
	s_waitcnt lgkmcnt(0)
	s_barrier
	s_waitcnt lgkmcnt(0)
	v_mfma_scale_f32_16x16x128_f8f6f4 v[158:161], v[18:25], v[168:175], v[158:161], v180, v180 op_sel_hi:[0,0,0]
	v_mfma_scale_f32_16x16x128_f8f6f4 v[154:157], v[26:33], v[168:175], v[154:157], v180, v180 op_sel_hi:[0,0,0]
	v_mfma_scale_f32_16x16x128_f8f6f4 v[142:145], v[18:25], v[184:191], v[142:145], v180, v180 op_sel_hi:[0,0,0]
	v_mfma_scale_f32_16x16x128_f8f6f4 v[138:141], v[26:33], v[184:191], v[138:141], v180, v180 op_sel_hi:[0,0,0]
	v_mfma_scale_f32_16x16x128_f8f6f4 v[126:129], v[18:25], v[192:199], v[126:129], v180, v180 op_sel_hi:[0,0,0]
	v_mfma_scale_f32_16x16x128_f8f6f4 v[122:125], v[26:33], v[192:199], v[122:125], v180, v180 op_sel_hi:[0,0,0]
	v_mfma_scale_f32_16x16x128_f8f6f4 v[110:113], v[18:25], v[200:207], v[110:113], v180, v180 op_sel_hi:[0,0,0]
	v_mfma_scale_f32_16x16x128_f8f6f4 v[106:109], v[26:33], v[200:207], v[106:109], v180, v180 op_sel_hi:[0,0,0]
	v_mfma_scale_f32_16x16x128_f8f6f4 v[150:153], v[2:9], v[168:175], v[150:153], v180, v180 op_sel_hi:[0,0,0]
	v_mfma_scale_f32_16x16x128_f8f6f4 v[146:149], v[10:17], v[168:175], v[146:149], v180, v180 op_sel_hi:[0,0,0]
	v_mfma_scale_f32_16x16x128_f8f6f4 v[134:137], v[2:9], v[184:191], v[134:137], v180, v180 op_sel_hi:[0,0,0]
	v_mfma_scale_f32_16x16x128_f8f6f4 v[130:133], v[10:17], v[184:191], v[130:133], v180, v180 op_sel_hi:[0,0,0]
	v_mfma_scale_f32_16x16x128_f8f6f4 v[118:121], v[2:9], v[192:199], v[118:121], v180, v180 op_sel_hi:[0,0,0]
	v_mfma_scale_f32_16x16x128_f8f6f4 v[114:117], v[10:17], v[192:199], v[114:117], v180, v180 op_sel_hi:[0,0,0]
	v_mfma_scale_f32_16x16x128_f8f6f4 v[102:105], v[2:9], v[200:207], v[102:105], v180, v180 op_sel_hi:[0,0,0]
	v_mfma_scale_f32_16x16x128_f8f6f4 v[98:101], v[10:17], v[200:207], v[98:101], v180, v180 op_sel_hi:[0,0,0]
	s_barrier
	s_add_i32 s80, s80, s62
	v_lshl_add_u64 v[168:169], s[58:59], 0, v[0:1]
	s_mov_b32 m0, s80
	ds_read_b128 v[184:187], v183 offset:16384
	ds_read_b128 v[188:191], v183 offset:17408
	ds_read_b128 v[192:195], v183 offset:18432
	ds_read_b128 v[196:199], v183 offset:19456
	ds_read_b128 v[200:203], v183 offset:20480
	ds_read_b128 v[204:207], v183 offset:21504
	ds_read_b128 v[212:215], v183 offset:22528
	ds_read_b128 v[216:219], v183 offset:23552
	global_load_lds_dwordx4 v[168:169], off
	s_add_i32 m0, s80, 0x2000
	s_add_u32 s58, s58, s8
	s_addc_u32 s59, s59, s9
	v_lshl_add_u64 v[170:171], v[168:169], 0, s[6:7]
	v_lshl_add_u64 v[172:173], s[58:59], 0, v[0:1]
	s_add_i32 s58, s81, s62
	global_load_lds_dwordx4 v[170:171], off
	s_mov_b32 m0, s58
	v_lshl_add_u64 v[174:175], v[172:173], 0, s[6:7]
	global_load_lds_dwordx4 v[172:173], off
	s_add_i32 m0, s58, 0x2000
	v_lshl_add_u64 v[176:177], s[56:57], 0, v[162:163]
	global_load_lds_dwordx4 v[174:175], off
	s_mov_b32 m0, s64
	v_lshl_add_u64 v[178:179], v[176:177], 0, s[10:11]
	global_load_lds_dwordx4 v[176:177], off
	s_mov_b32 m0, s65
	s_nop 0
	global_load_lds_dwordx4 v[178:179], off
	s_waitcnt vmcnt(8)
	s_waitcnt lgkmcnt(0)
	s_barrier
	s_waitcnt lgkmcnt(0)
	v_mfma_scale_f32_16x16x128_f8f6f4 v[94:97], v[18:25], v[184:191], v[94:97], v180, v180 op_sel_hi:[0,0,0]
	v_mfma_scale_f32_16x16x128_f8f6f4 v[90:93], v[26:33], v[184:191], v[90:93], v180, v180 op_sel_hi:[0,0,0]
	v_mfma_scale_f32_16x16x128_f8f6f4 v[78:81], v[18:25], v[192:199], v[78:81], v180, v180 op_sel_hi:[0,0,0]
	v_mfma_scale_f32_16x16x128_f8f6f4 v[74:77], v[26:33], v[192:199], v[74:77], v180, v180 op_sel_hi:[0,0,0]
	v_mfma_scale_f32_16x16x128_f8f6f4 v[62:65], v[18:25], v[200:207], v[62:65], v180, v180 op_sel_hi:[0,0,0]
	v_mfma_scale_f32_16x16x128_f8f6f4 v[58:61], v[26:33], v[200:207], v[58:61], v180, v180 op_sel_hi:[0,0,0]
	v_mfma_scale_f32_16x16x128_f8f6f4 v[46:49], v[18:25], v[212:219], v[46:49], v180, v180 op_sel_hi:[0,0,0]
	v_mfma_scale_f32_16x16x128_f8f6f4 v[42:45], v[26:33], v[212:219], v[42:45], v180, v180 op_sel_hi:[0,0,0]
	v_mfma_scale_f32_16x16x128_f8f6f4 v[86:89], v[2:9], v[184:191], v[86:89], v180, v180 op_sel_hi:[0,0,0]
	v_mfma_scale_f32_16x16x128_f8f6f4 v[82:85], v[10:17], v[184:191], v[82:85], v180, v180 op_sel_hi:[0,0,0]
	v_mfma_scale_f32_16x16x128_f8f6f4 v[70:73], v[2:9], v[192:199], v[70:73], v180, v180 op_sel_hi:[0,0,0]
	v_mfma_scale_f32_16x16x128_f8f6f4 v[66:69], v[10:17], v[192:199], v[66:69], v180, v180 op_sel_hi:[0,0,0]
	v_mfma_scale_f32_16x16x128_f8f6f4 v[54:57], v[2:9], v[200:207], v[54:57], v180, v180 op_sel_hi:[0,0,0]
	v_mfma_scale_f32_16x16x128_f8f6f4 v[50:53], v[10:17], v[200:207], v[50:53], v180, v180 op_sel_hi:[0,0,0]
	v_mfma_scale_f32_16x16x128_f8f6f4 v[38:41], v[2:9], v[212:219], v[38:41], v180, v180 op_sel_hi:[0,0,0]
	v_mfma_scale_f32_16x16x128_f8f6f4 v[34:37], v[10:17], v[212:219], v[34:37], v180, v180 op_sel_hi:[0,0,0]
	s_barrier
	s_add_i32 s58, 0, 0x18000
	s_add_i32 s59, 0, 0x1c000
	v_add_u32_e32 v14, s58, v182
	v_add_u32_e32 v30, s59, v182
	ds_read_b128 v[2:5], v14
	ds_read_b128 v[6:9], v14 offset:1024
	ds_read_b128 v[10:13], v14 offset:2048
	ds_read_b128 v[14:17], v14 offset:3072
	ds_read_b128 v[18:21], v30
	ds_read_b128 v[22:25], v30 offset:1024
	ds_read_b128 v[26:29], v30 offset:2048
	ds_read_b128 v[30:33], v30 offset:3072
	s_add_u32 s56, s56, s6
	s_addc_u32 s57, s57, s7
	s_mov_b32 m0, s66
	v_lshl_add_u64 v[208:209], s[56:57], 0, v[162:163]
	ds_read_b128 v[184:187], v183 offset:32768
	ds_read_b128 v[188:191], v183 offset:33792
	ds_read_b128 v[192:195], v183 offset:34816
	ds_read_b128 v[196:199], v183 offset:35840
	ds_read_b128 v[200:203], v183 offset:36864
	ds_read_b128 v[204:207], v183 offset:37888
	ds_read_b128 v[212:215], v183 offset:38912
	ds_read_b128 v[216:219], v183 offset:39936
	global_load_lds_dwordx4 v[208:209], off
	v_lshl_add_u64 v[208:209], v[208:209], 0, s[10:11]
	s_mov_b32 m0, s67
	s_nop 0
	global_load_lds_dwordx4 v[208:209], off
	s_waitcnt vmcnt(8)
	s_waitcnt lgkmcnt(0)
	s_barrier
	s_waitcnt lgkmcnt(0)
	v_mfma_scale_f32_16x16x128_f8f6f4 v[158:161], v[2:9], v[184:191], v[158:161], v180, v180 op_sel_hi:[0,0,0]
	v_mfma_scale_f32_16x16x128_f8f6f4 v[154:157], v[10:17], v[184:191], v[154:157], v180, v180 op_sel_hi:[0,0,0]
	v_mfma_scale_f32_16x16x128_f8f6f4 v[142:145], v[2:9], v[192:199], v[142:145], v180, v180 op_sel_hi:[0,0,0]
	v_mfma_scale_f32_16x16x128_f8f6f4 v[138:141], v[10:17], v[192:199], v[138:141], v180, v180 op_sel_hi:[0,0,0]
	v_mfma_scale_f32_16x16x128_f8f6f4 v[126:129], v[2:9], v[200:207], v[126:129], v180, v180 op_sel_hi:[0,0,0]
	v_mfma_scale_f32_16x16x128_f8f6f4 v[122:125], v[10:17], v[200:207], v[122:125], v180, v180 op_sel_hi:[0,0,0]
	v_mfma_scale_f32_16x16x128_f8f6f4 v[110:113], v[2:9], v[212:219], v[110:113], v180, v180 op_sel_hi:[0,0,0]
	v_mfma_scale_f32_16x16x128_f8f6f4 v[106:109], v[10:17], v[212:219], v[106:109], v180, v180 op_sel_hi:[0,0,0]
	v_mfma_scale_f32_16x16x128_f8f6f4 v[150:153], v[18:25], v[184:191], v[150:153], v180, v180 op_sel_hi:[0,0,0]
	v_mfma_scale_f32_16x16x128_f8f6f4 v[146:149], v[26:33], v[184:191], v[146:149], v180, v180 op_sel_hi:[0,0,0]
	v_mfma_scale_f32_16x16x128_f8f6f4 v[134:137], v[18:25], v[192:199], v[134:137], v180, v180 op_sel_hi:[0,0,0]
	v_mfma_scale_f32_16x16x128_f8f6f4 v[130:133], v[26:33], v[192:199], v[130:133], v180, v180 op_sel_hi:[0,0,0]
	v_mfma_scale_f32_16x16x128_f8f6f4 v[118:121], v[18:25], v[200:207], v[118:121], v180, v180 op_sel_hi:[0,0,0]
	v_mfma_scale_f32_16x16x128_f8f6f4 v[114:117], v[26:33], v[200:207], v[114:117], v180, v180 op_sel_hi:[0,0,0]
	v_mfma_scale_f32_16x16x128_f8f6f4 v[102:105], v[18:25], v[212:219], v[102:105], v180, v180 op_sel_hi:[0,0,0]
	v_mfma_scale_f32_16x16x128_f8f6f4 v[98:101], v[26:33], v[212:219], v[98:101], v180, v180 op_sel_hi:[0,0,0]
	s_barrier
	s_add_i32 s56, s58, s62
	v_lshl_add_u64 v[168:169], v[168:169], 0, s[36:37]
	s_mov_b32 m0, s56
	ds_read_b128 v[184:187], v183 offset:49152
	ds_read_b128 v[188:191], v183 offset:50176
	ds_read_b128 v[192:195], v183 offset:51200
	ds_read_b128 v[196:199], v183 offset:52224
	ds_read_b128 v[200:203], v183 offset:53248
	ds_read_b128 v[204:207], v183 offset:54272
	ds_read_b128 v[212:215], v183 offset:55296
	ds_read_b128 v[216:219], v183 offset:56320
	global_load_lds_dwordx4 v[168:169], off
	v_lshl_add_u64 v[168:169], v[170:171], 0, s[36:37]
	s_add_i32 m0, s56, 0x2000
	s_add_i32 s56, s59, s62
	global_load_lds_dwordx4 v[168:169], off
	v_lshl_add_u64 v[168:169], v[172:173], 0, s[36:37]
	s_mov_b32 m0, s56
	s_nop 0
	global_load_lds_dwordx4 v[168:169], off
	v_lshl_add_u64 v[168:169], v[174:175], 0, s[36:37]
	s_add_i32 m0, s56, 0x2000
	s_nop 0
	global_load_lds_dwordx4 v[168:169], off
	v_lshl_add_u64 v[168:169], v[176:177], 0, s[36:37]
	s_mov_b32 m0, s69
	s_nop 0
	global_load_lds_dwordx4 v[168:169], off
	v_lshl_add_u64 v[168:169], v[178:179], 0, s[36:37]
	s_mov_b32 m0, s72
	s_nop 0
	global_load_lds_dwordx4 v[168:169], off
	s_waitcnt vmcnt(8)
	s_waitcnt lgkmcnt(0)
	s_barrier
	s_waitcnt lgkmcnt(0)
	v_mfma_scale_f32_16x16x128_f8f6f4 v[94:97], v[2:9], v[184:191], v[94:97], v180, v180 op_sel_hi:[0,0,0]
	v_mfma_scale_f32_16x16x128_f8f6f4 v[90:93], v[10:17], v[184:191], v[90:93], v180, v180 op_sel_hi:[0,0,0]
	v_mfma_scale_f32_16x16x128_f8f6f4 v[78:81], v[2:9], v[192:199], v[78:81], v180, v180 op_sel_hi:[0,0,0]
	v_mfma_scale_f32_16x16x128_f8f6f4 v[74:77], v[10:17], v[192:199], v[74:77], v180, v180 op_sel_hi:[0,0,0]
	v_mfma_scale_f32_16x16x128_f8f6f4 v[62:65], v[2:9], v[200:207], v[62:65], v180, v180 op_sel_hi:[0,0,0]
	v_mfma_scale_f32_16x16x128_f8f6f4 v[58:61], v[10:17], v[200:207], v[58:61], v180, v180 op_sel_hi:[0,0,0]
	v_mfma_scale_f32_16x16x128_f8f6f4 v[46:49], v[2:9], v[212:219], v[46:49], v180, v180 op_sel_hi:[0,0,0]
	v_mfma_scale_f32_16x16x128_f8f6f4 v[42:45], v[10:17], v[212:219], v[42:45], v180, v180 op_sel_hi:[0,0,0]
	v_mfma_scale_f32_16x16x128_f8f6f4 v[86:89], v[18:25], v[184:191], v[86:89], v180, v180 op_sel_hi:[0,0,0]
	v_mfma_scale_f32_16x16x128_f8f6f4 v[82:85], v[26:33], v[184:191], v[82:85], v180, v180 op_sel_hi:[0,0,0]
	v_mfma_scale_f32_16x16x128_f8f6f4 v[70:73], v[18:25], v[192:199], v[70:73], v180, v180 op_sel_hi:[0,0,0]
	v_mfma_scale_f32_16x16x128_f8f6f4 v[66:69], v[26:33], v[192:199], v[66:69], v180, v180 op_sel_hi:[0,0,0]
	v_mfma_scale_f32_16x16x128_f8f6f4 v[54:57], v[18:25], v[200:207], v[54:57], v180, v180 op_sel_hi:[0,0,0]
	v_mfma_scale_f32_16x16x128_f8f6f4 v[50:53], v[26:33], v[200:207], v[50:53], v180, v180 op_sel_hi:[0,0,0]
	v_mfma_scale_f32_16x16x128_f8f6f4 v[38:41], v[18:25], v[212:219], v[38:41], v180, v180 op_sel_hi:[0,0,0]
	v_mfma_scale_f32_16x16x128_f8f6f4 v[34:37], v[26:33], v[212:219], v[34:37], v180, v180 op_sel_hi:[0,0,0]
	s_barrier
	s_add_u32 s54, s54, 0x100
	s_addc_u32 s55, s55, 0
	s_add_u32 s70, s70, 0x100
	s_addc_u32 s78, s78, 0
	s_cmp_ge_i32 s79, s30
	s_mov_b32 s56, s79
	s_cbranch_scc0 .LBB0_145
	v_readlane_b32 s70, v254, 49

.LBB0_205:
	s_setprio 0
	v_readlane_b32 s8, v252, 1
	v_readlane_b32 s10, v252, 3
	s_cmp_le_i32 s10, s12
	s_cselect_b64 s[4:5], -1, 0
	s_and_b64 s[4:5], s[4:5], s[6:7]
	v_writelane_b32 v254, s4, 53
	s_andn2_b64 vcc, exec, s[4:5]
	v_readlane_b32 s9, v252, 2
	v_writelane_b32 v254, s5, 54
	v_readlane_b32 s11, v252, 4
	s_cbranch_vccnz .LBB0_402
	v_readlane_b32 s4, v252, 6
	v_mbcnt_lo_u32_b32 v142, -1, 0
	v_mbcnt_hi_u32_b32 v142, -1, v142
	v_readlane_b32 s27, v252, 0
	v_readlane_b32 s5, v252, 7
	s_load_dwordx2 s[6:7], s[4:5], 0xe0
	s_waitcnt lgkmcnt(0)
	v_writelane_b32 v254, s6, 55
	s_nop 1
	v_writelane_b32 v254, s7, 56
	s_load_dword s6, s[4:5], 0xf0
	s_load_dwordx8 s[40:47], s[4:5], 0x10
	s_waitcnt lgkmcnt(0)
	s_bitcmp0_b32 s6, 0
	v_writelane_b32 v254, s40, 57
	s_nop 1
	v_writelane_b32 v254, s41, 58
	v_writelane_b32 v254, s42, 59
	v_writelane_b32 v254, s43, 60
	v_writelane_b32 v254, s44, 61
	v_writelane_b32 v254, s45, 62
	v_writelane_b32 v254, s46, 63
	v_writelane_b32 v255, s47, 0
	s_load_dwordx8 s[40:47], s[4:5], 0x38
	s_waitcnt lgkmcnt(0)
	v_writelane_b32 v255, s40, 1
	s_nop 1
	v_writelane_b32 v255, s41, 2
	v_writelane_b32 v255, s42, 3
	v_writelane_b32 v255, s43, 4
	v_writelane_b32 v255, s44, 5
	v_writelane_b32 v255, s45, 6
	v_writelane_b32 v255, s46, 7
	v_writelane_b32 v255, s47, 8
	v_writelane_b32 v255, s6, 9
	v_readlane_b32 s6, v252, 10
	s_nop 1
	v_add_u32_e32 v178, s6, v142
	s_cbranch_scc1 .LBB0_284
	v_readlane_b32 s6, v253, 37
	s_cmp_ge_i32 s27, s6
	s_mov_b32 s75, s31
	s_cbranch_scc0 .LBB0_259
	v_readlane_b32 s6, v253, 37
	s_sub_i32 s6, s27, s6
	s_lshl_b32 s10, s6, 3
	v_readlane_b32 s6, v252, 5
	s_add_i32 s10, s10, s6
	s_cmpk_gt_u32 s10, 0xc2ff
	s_cbranch_scc1 .LBB0_259
	s_load_dwordx8 s[40:47], s[4:5], 0x98
	s_load_dwordx4 s[52:55], s[4:5], 0xb8
	s_lshl_b64 s[4:5], s[74:75], 28
	s_mul_i32 s6, s10, 0xaaab
	s_waitcnt lgkmcnt(0)
	s_add_u32 s12, s40, s4
	s_addc_u32 s18, s41, s5
	s_add_u32 s20, s42, s4
	s_addc_u32 s21, s43, s5
	s_add_u32 s48, s44, s4
	s_addc_u32 s49, s45, s5
	s_lshl_b64 s[4:5], s[74:75], 22
	s_add_u32 s50, s46, s4
	s_addc_u32 s51, s47, s5
	s_add_u32 s52, s52, s4
	s_addc_u32 s53, s53, s5
	s_add_u32 s54, s54, s4
	s_addc_u32 s55, s55, s5
	s_lshr_b32 s30, s6, 25
	s_mul_i32 s4, s30, 0x300
	s_sub_i32 s4, s10, s4
	s_and_b32 s11, s4, 0xffff
	s_bfe_u32 s38, s4, 0x80008
	s_cmpk_gt_u32 s11, 0xff
	s_mov_b64 s[4:5], -1
	s_cbranch_scc0 .LBB0_215
	s_cmpk_lt_u32 s10, 0xc000
	s_cselect_b64 s[4:5], -1, 0
	s_lshl_b32 s39, s30, 22
	s_cmp_lg_u32 s38, 1
	s_mov_b64 s[8:9], -1
	s_cbranch_scc0 .LBB0_212
	s_add_u32 s8, s48, s39
	s_addc_u32 s9, s49, 0
	s_and_b64 s[6:7], s[4:5], exec
	s_cselect_b32 s7, s9, s55
	s_cselect_b32 s6, s8, s54
	s_mov_b64 s[8:9], 0
